# speedup vs baseline: 1.0283x; 1.0089x over previous
.LBB7_11:
	s_mov_b64 s[26:27], 0x80
	s_and_b32 s22, s20, 3
	s_add_i32 m0, s43, 0x18000
	v_lshl_add_u64 v[8:9], v[8:9], 0, s[26:27]
	s_lshl_b32 s48, s21, 6
	s_lshl_b32 s21, s21, 13
	s_lshl_b32 s23, s22, 12
	s_waitcnt vmcnt(4)
	s_barrier
	global_load_lds_dwordx4 v[8:9], off
	v_lshl_add_u64 v[6:7], v[6:7], 0, s[26:27]
	s_add_i32 m0, s43, 0x1a000
	s_add_i32 s49, s43, 0x8000
	s_add_i32 s50, s43, 0xa000
	global_load_lds_dwordx4 v[6:7], off
	v_lshl_add_u64 v[4:5], v[4:5], 0, s[26:27]
	s_mov_b32 m0, s49
	s_add_u32 s0, s30, 0xc080
	global_load_lds_dwordx4 v[4:5], off
	v_lshl_add_u64 v[2:3], v[2:3], 0, s[26:27]
	s_mov_b32 m0, s50
	s_addc_u32 s1, s31, 0
	global_load_lds_dwordx4 v[2:3], off
	s_add_i32 m0, s43, 0x1c000
	v_lshl_add_u64 v[2:3], s[0:1], 0, v[146:147]
	global_load_lds_dwordx4 v[2:3], off
	v_lshl_add_u64 v[2:3], s[0:1], 0, v[150:151]
	s_add_i32 m0, s43, 0x1e000
	s_lshl_b32 s53, s33, 2
	global_load_lds_dwordx4 v[2:3], off
	s_abs_i32 s54, s53
	v_cvt_f32_u32_e32 v6, s54
	v_and_b32_e32 v165, 15, v0
	v_and_b32_e32 v2, 48, v0
	v_lshlrev_b32_e32 v4, 2, v0
	v_rcp_iflag_f32_e32 v6, v6
	v_lshlrev_b32_e32 v5, 6, v0
	v_bfe_u32 v167, v0, 3, 3
	v_and_b32_e32 v0, 7, v0
	s_abs_i32 s57, s33
	v_lshlrev_b32_e32 v168, 4, v0
	v_add_lshl_u32 v169, v0, s10, 4
	v_mul_f32_e32 v0, 0x4f7ffffe, v6
	v_cvt_f32_u32_e32 v6, s57
	s_movk_i32 s0, 0x3c0
	s_mulk_i32 s20, 0x900
	v_cvt_u32_f32_e32 v0, v0
	v_rcp_iflag_f32_e32 v6, v6
	v_and_or_b32 v5, v5, s0, v2
	s_add_i32 s0, s20, 0
	v_lshl_or_b32 v3, v165, 6, v2
	v_and_b32_e32 v4, 32, v4
	s_add_i32 s0, s0, 0x20000
	v_bitop3_b32 v3, v3, s21, v4 bitop3:0xde
	v_bitop3_b32 v166, s23, v5, v4 bitop3:0xf6
	s_movk_i32 s1, 0x90
	v_mov_b32_e32 v4, s0
	v_mad_u32_u24 v5, v165, s1, v4
	v_mad_u32_u24 v4, v167, s1, v4
	v_readfirstlane_b32 s1, v0
	v_mul_f32_e32 v0, 0x4f7ffffe, v6
	v_cvt_u32_f32_e32 v0, v0
	s_sub_i32 s0, 0, s54
	s_mul_i32 s0, s0, s1
	s_mul_hi_u32 s0, s1, s0
	s_add_i32 s59, s1, s0
	s_sub_i32 s0, 0, s57
	v_readfirstlane_b32 s1, v0
	s_waitcnt vmcnt(6)
	s_mul_i32 s0, s0, s1
	v_add_u16_e32 v0, v1, v10
	s_mul_hi_u32 s0, s1, s0
	v_lshrrev_b16_e32 v0, 1, v0
	s_add_i32 s65, 0, 0x10000
	s_add_i32 s66, 0, 0x14000
	s_mov_b32 s23, 0x20000
	s_lshl_b32 s51, s22, 6
	s_waitcnt lgkmcnt(0)
	s_ashr_i32 s52, s11, 31
	s_lshl_b32 s22, s10, 17
	s_and_b32 s21, s9, 0xffff
	s_mov_b32 s20, s8
	s_lshl_b32 s55, s10, 5
	s_mul_i32 s56, s10, 48
	s_bfe_i32 s58, s33, 0x1001c
	s_ashr_i32 s60, s33, 31
	s_add_i32 s61, s1, s0
	s_mul_i32 s62, s10, 0xc0
	s_mul_i32 s63, s10, 0x60
	s_lshl_b32 s64, s10, 4
	v_add_lshl_u32 v152, v11, v0, 1
	v_mov_b32_e32 v153, v147
	v_add_lshl_u32 v154, v12, v0, 1
	v_mov_b32_e32 v155, v147
	v_mov_b64_e32 v[156:157], s[6:7]
	v_add_u32_e32 v170, s65, v166
	v_add_u32_e32 v171, 0, v3
	v_add_u32_e32 v172, s66, v166
	v_add_u32_e32 v173, v5, v2
	v_add_u32_e32 v174, v4, v168
	s_barrier
	s_cmpk_gt_u32 s36, 0xff
	s_cbranch_scc0 .Lprio7_done
.Lprio7_done:
.LBB7_12:
	s_add_i32 s47, s47, 1
	s_mul_i32 s0, s47, s52
	s_mul_hi_u32 s1, s47, s11
	s_add_i32 s1, s1, s0
	s_mul_i32 s0, s47, s11
	s_add_u32 s0, s0, s2
	s_addc_u32 s1, s1, s39
	v_cmp_ge_i64_e32 vcc, s[0:1], v[156:157]
	s_and_b64 s[6:7], exec, vcc
	s_mov_b64 vcc, s[6:7]
	s_cbranch_vccnz .LBB7_22
	s_ashr_i32 s8, s0, 31
	s_lshr_b32 s8, s8, 29
	s_add_i32 s34, s0, s8
	s_and_b32 s8, s34, -8
	s_sub_i32 s35, s0, s8
	s_cmp_ge_i32 s35, s38
	s_mov_b64 s[8:9], -1
	s_cbranch_scc0 .LBB7_15
	s_sub_i32 s8, s35, s38
	s_mul_i32 s8, s8, s37
	s_add_i32 s68, s8, s41
	s_mov_b64 s[8:9], 0

.LBB7_32:
	s_endpgm
	s_endpgm
	s_endpgm
	s_endpgm
	s_endpgm
	.section	.rodata,"a",@progbits
	.p2align	6, 0x0

.LBB8_11:
	s_mov_b64 s[36:37], 0x80
	s_and_b32 s34, s24, 3
	s_add_i32 m0, s51, 0x18000
	v_lshl_add_u64 v[8:9], v[8:9], 0, s[36:37]
	s_lshl_b32 s58, s25, 6
	s_lshl_b32 s25, s25, 13
	s_lshl_b32 s26, s34, 12
	s_waitcnt vmcnt(4)
	s_barrier
	global_load_lds_dwordx4 v[8:9], off
	v_lshl_add_u64 v[6:7], v[6:7], 0, s[36:37]
	s_add_i32 m0, s51, 0x1a000
	s_add_i32 s59, s51, 0x8000
	s_add_i32 s60, s51, 0xa000
	global_load_lds_dwordx4 v[6:7], off
	v_lshl_add_u64 v[4:5], v[4:5], 0, s[36:37]
	s_mov_b32 m0, s59
	s_add_u32 s0, s40, 0xc080
	global_load_lds_dwordx4 v[4:5], off
	v_lshl_add_u64 v[2:3], v[2:3], 0, s[36:37]
	s_mov_b32 m0, s60
	s_addc_u32 s1, s41, 0
	global_load_lds_dwordx4 v[2:3], off
	s_add_i32 m0, s51, 0x1c000
	v_lshl_add_u64 v[2:3], s[0:1], 0, v[178:179]
	global_load_lds_dwordx4 v[2:3], off
	v_lshl_add_u64 v[2:3], s[0:1], 0, v[182:183]
	s_add_i32 m0, s51, 0x1e000
	s_lshl_b32 s62, s33, 3
	global_load_lds_dwordx4 v[2:3], off
	s_abs_i32 s63, s62
	v_and_b32_e32 v227, 15, v0
	v_and_b32_e32 v2, 48, v0
	v_lshlrev_b32_e32 v4, 2, v0
	v_lshlrev_b32_e32 v5, 6, v0
	v_bfe_u32 v229, v0, 3, 3
	v_cvt_f32_u32_e32 v0, s63
	s_abs_i32 s65, s33
	v_cvt_f32_u32_e32 v6, s65
	s_movk_i32 s0, 0x3c0
	v_rcp_iflag_f32_e32 v0, v0
	s_mulk_i32 s24, 0x900
	v_rcp_iflag_f32_e32 v6, v6
	v_and_or_b32 v5, v5, s0, v2
	v_mul_f32_e32 v0, 0x4f7ffffe, v0
	v_cvt_u32_f32_e32 v0, v0
	s_add_i32 s0, s24, 0
	v_lshl_or_b32 v3, v227, 6, v2
	v_and_b32_e32 v4, 32, v4
	s_add_i32 s0, s0, 0x20000
	v_bitop3_b32 v3, v3, s25, v4 bitop3:0xde
	v_bitop3_b32 v228, s26, v5, v4 bitop3:0xf6
	s_movk_i32 s1, 0x90
	v_mov_b32_e32 v4, s0
	v_mad_u32_u24 v5, v227, s1, v4
	v_mad_u32_u24 v4, v229, s1, v4
	v_readfirstlane_b32 s1, v0
	v_mul_f32_e32 v0, 0x4f7ffffe, v6
	v_cvt_u32_f32_e32 v0, v0
	s_sub_i32 s0, 0, s63
	s_mul_i32 s0, s0, s1
	s_mul_hi_u32 s0, s1, s0
	s_add_i32 s67, s1, s0
	s_sub_i32 s0, 0, s65
	v_readfirstlane_b32 s1, v0
	v_add_u16_e32 v0, v1, v10
	s_waitcnt vmcnt(6)
	s_mul_i32 s0, s0, s1
	v_lshrrev_b16_e32 v0, 1, v0
	v_and_b32_e32 v230, 0x70, v13
	s_mul_hi_u32 s0, s1, s0
	v_add_lshl_u32 v184, v11, v0, 1
	v_add_lshl_u32 v186, v12, v0, 1
	s_add_i32 s70, 0, 0x10000
	s_add_i32 s71, 0, 0x14000
	v_mbcnt_lo_u32_b32 v0, -1, 0
	s_mov_b32 s27, 0x20000
	s_lshl_b32 s61, s34, 6
	s_waitcnt lgkmcnt(0)
	s_ashr_i32 s64, s55, 31
	s_mov_b32 s26, 0x6000000
	s_and_b32 s25, s9, 0xffff
	s_mov_b32 s24, s8
	s_bfe_i32 s66, s33, 0x1001c
	s_ashr_i32 s68, s33, 31
	s_add_i32 s69, s1, s0
	v_mov_b32_e32 v185, v179
	v_mov_b32_e32 v187, v179
	v_mov_b64_e32 v[188:189], s[6:7]
	v_add_u32_e32 v231, s70, v228
	v_add_u32_e32 v232, 0, v3
	v_add_u32_e32 v233, s71, v228
	s_movk_i32 s72, 0x600
	v_mbcnt_hi_u32_b32 v234, -1, v0
	v_add_u32_e32 v235, v5, v2
	v_add_u32_e32 v236, v4, v230
	s_movk_i32 s73, 0x60
	s_mov_b32 s74, 0x30000
	s_mov_b32 s75, 0x36000
	s_lshl_b32 s34, s34, 3
	s_movk_i32 s76, 0x3000
	s_mov_b32 s77, 0x3c000
	s_mov_b32 s78, 0x42000
	s_movk_i32 s79, 0x1000
	s_mov_b32 s80, s35
	s_barrier
	s_cmpk_gt_u32 s44, 0xff
	s_cbranch_scc0 .Lprio8_done
.Lprio8_done:
.LBB8_12:
	s_add_i32 s80, s80, 1
	s_mul_i32 s0, s80, s64
	s_mul_hi_u32 s1, s80, s55
	s_add_i32 s1, s1, s0
	s_mul_i32 s0, s80, s55
	s_add_u32 s0, s0, s2
	s_addc_u32 s1, s1, s47
	v_cmp_ge_i64_e32 vcc, s[0:1], v[188:189]
	s_and_b64 s[6:7], exec, vcc
	s_mov_b64 vcc, s[6:7]
	s_cbranch_vccnz .LBB8_22
	s_ashr_i32 s8, s0, 31
	s_lshr_b32 s8, s8, 29
	s_add_i32 s42, s0, s8
	s_and_b32 s8, s42, -8
	s_sub_i32 s43, s0, s8
	s_cmp_ge_i32 s43, s46
	s_mov_b64 s[8:9], -1
	s_cbranch_scc0 .LBB8_15
	s_sub_i32 s8, s43, s46
	s_mul_i32 s8, s8, s45
	s_add_i32 s81, s8, s49
	s_mov_b64 s[8:9], 0

.LBB8_32:
	s_endpgm
	s_endpgm
	s_endpgm
	s_endpgm
	s_endpgm
	s_endpgm
	s_endpgm
	s_endpgm
	s_endpgm
	s_endpgm
	s_endpgm
	s_endpgm
	s_endpgm
	s_endpgm
	s_endpgm
	s_endpgm
	s_endpgm
	s_endpgm
	s_endpgm
	s_endpgm
	s_endpgm
	s_endpgm
	s_endpgm
	s_endpgm
	s_endpgm
	s_endpgm
	s_endpgm
	s_endpgm
	s_endpgm
	s_endpgm
	s_endpgm
	s_endpgm
	s_endpgm
	s_endpgm
	s_endpgm
	s_endpgm
	s_endpgm
	s_endpgm
	s_endpgm
	s_endpgm
	s_endpgm
	s_endpgm
	s_endpgm
	s_endpgm
	s_endpgm
	s_endpgm
	s_endpgm
	s_endpgm
	s_endpgm
	s_endpgm
	s_endpgm
	s_endpgm
	s_endpgm
	s_endpgm
	s_endpgm
	s_endpgm
	s_endpgm
	s_endpgm
	s_endpgm
	s_endpgm
	s_endpgm
	s_endpgm
	s_endpgm
	s_endpgm

.LBB9_11:
	s_mov_b64 s[26:27], 0x80
	s_and_b32 s22, s20, 3
	s_add_i32 m0, s43, 0x18000
	v_lshl_add_u64 v[8:9], v[8:9], 0, s[26:27]
	s_lshl_b32 s48, s21, 6
	s_lshl_b32 s21, s21, 13
	s_lshl_b32 s23, s22, 12
	s_waitcnt vmcnt(4)
	s_barrier
	global_load_lds_dwordx4 v[8:9], off
	v_lshl_add_u64 v[6:7], v[6:7], 0, s[26:27]
	s_add_i32 m0, s43, 0x1a000
	s_add_i32 s49, s43, 0x8000
	s_add_i32 s50, s43, 0xa000
	global_load_lds_dwordx4 v[6:7], off
	v_lshl_add_u64 v[4:5], v[4:5], 0, s[26:27]
	s_mov_b32 m0, s49
	s_add_u32 s0, s30, 0xc080
	global_load_lds_dwordx4 v[4:5], off
	v_lshl_add_u64 v[2:3], v[2:3], 0, s[26:27]
	s_mov_b32 m0, s50
	s_addc_u32 s1, s31, 0
	global_load_lds_dwordx4 v[2:3], off
	s_add_i32 m0, s43, 0x1c000
	v_lshl_add_u64 v[2:3], s[0:1], 0, v[146:147]
	global_load_lds_dwordx4 v[2:3], off
	v_lshl_add_u64 v[2:3], s[0:1], 0, v[150:151]
	s_add_i32 m0, s43, 0x1e000
	s_lshl_b32 s53, s33, 2
	global_load_lds_dwordx4 v[2:3], off
	s_abs_i32 s54, s53
	v_cvt_f32_u32_e32 v6, s54
	v_and_b32_e32 v167, 15, v0
	v_and_b32_e32 v2, 48, v0
	v_lshlrev_b32_e32 v4, 2, v0
	v_rcp_iflag_f32_e32 v6, v6
	v_lshlrev_b32_e32 v5, 6, v0
	v_bfe_u32 v169, v0, 3, 3
	v_and_b32_e32 v0, 7, v0
	s_abs_i32 s57, s33
	v_lshlrev_b32_e32 v170, 4, v0
	v_add_lshl_u32 v171, v0, s10, 4
	v_mul_f32_e32 v0, 0x4f7ffffe, v6
	v_cvt_f32_u32_e32 v6, s57
	s_movk_i32 s0, 0x3c0
	s_mulk_i32 s20, 0x900
	v_cvt_u32_f32_e32 v0, v0
	v_rcp_iflag_f32_e32 v6, v6
	v_and_or_b32 v5, v5, s0, v2
	s_add_i32 s0, s20, 0
	v_lshl_or_b32 v3, v167, 6, v2
	v_and_b32_e32 v4, 32, v4
	s_add_i32 s0, s0, 0x20000
	v_bitop3_b32 v3, v3, s21, v4 bitop3:0xde
	v_bitop3_b32 v168, s23, v5, v4 bitop3:0xf6
	s_movk_i32 s1, 0x90
	v_mov_b32_e32 v4, s0
	v_mad_u32_u24 v5, v167, s1, v4
	v_mad_u32_u24 v4, v169, s1, v4
	v_readfirstlane_b32 s1, v0
	v_mul_f32_e32 v0, 0x4f7ffffe, v6
	v_cvt_u32_f32_e32 v0, v0
	s_sub_i32 s0, 0, s54
	s_mul_i32 s0, s0, s1
	s_mul_hi_u32 s0, s1, s0
	s_add_i32 s59, s1, s0
	s_sub_i32 s0, 0, s57
	v_readfirstlane_b32 s1, v0
	s_waitcnt vmcnt(6)
	s_mul_i32 s0, s0, s1
	v_add_u16_e32 v0, v1, v10
	s_mul_hi_u32 s0, s1, s0
	v_lshrrev_b16_e32 v0, 1, v0
	s_add_i32 s65, 0, 0x10000
	s_add_i32 s66, 0, 0x14000
	s_mov_b32 s23, 0x20000
	s_lshl_b32 s51, s22, 6
	s_waitcnt lgkmcnt(0)
	s_ashr_i32 s52, s11, 31
	s_lshl_b32 s22, s10, 17
	s_and_b32 s21, s9, 0xffff
	s_mov_b32 s20, s8
	s_lshl_b32 s55, s10, 5
	s_mul_i32 s56, s10, 48
	s_bfe_i32 s58, s33, 0x1001c
	s_ashr_i32 s60, s33, 31
	s_add_i32 s61, s1, s0
	s_mul_i32 s62, s10, 0xc0
	s_mul_i32 s63, s10, 0x60
	s_lshl_b32 s64, s10, 4
	v_add_lshl_u32 v152, v11, v0, 1
	v_mov_b32_e32 v153, v147
	v_add_lshl_u32 v154, v12, v0, 1
	v_mov_b32_e32 v155, v147
	v_mov_b64_e32 v[156:157], s[6:7]
	v_add_u32_e32 v172, s65, v168
	v_add_u32_e32 v173, 0, v3
	v_add_u32_e32 v174, s66, v168
	v_add_u32_e32 v175, v5, v2
	v_add_u32_e32 v176, v4, v170
	s_barrier
	s_cmpk_gt_u32 s36, 0xff
	s_cbranch_scc0 .Lprio9_done
.Lprio9_done:
.LBB9_12:
	s_add_i32 s47, s47, 1
	s_mul_i32 s0, s47, s52
	s_mul_hi_u32 s1, s47, s11
	s_add_i32 s1, s1, s0
	s_mul_i32 s0, s47, s11
	s_add_u32 s0, s0, s2
	s_addc_u32 s1, s1, s39
	v_cmp_ge_i64_e32 vcc, s[0:1], v[156:157]
	s_and_b64 s[6:7], exec, vcc
	s_mov_b64 vcc, s[6:7]
	s_cbranch_vccnz .LBB9_22
	s_ashr_i32 s8, s0, 31
	s_lshr_b32 s8, s8, 29
	s_add_i32 s34, s0, s8
	s_and_b32 s8, s34, -8
	s_sub_i32 s35, s0, s8
	s_cmp_ge_i32 s35, s38
	s_mov_b64 s[8:9], -1
	s_cbranch_scc0 .LBB9_15
	s_sub_i32 s8, s35, s38
	s_mul_i32 s8, s8, s37
	s_add_i32 s67, s8, s41
	s_mov_b64 s[8:9], 0

.LBB9_32:
	s_endpgm
	s_endpgm
	s_endpgm
	s_endpgm
	s_endpgm
	s_endpgm
	s_endpgm
	.section	.rodata,"a",@progbits
	.p2align	6, 0x0

.LBB10_11:
	s_mov_b64 s[36:37], 0x80
	s_and_b32 s34, s24, 3
	s_add_i32 m0, s51, 0x18000
	v_lshl_add_u64 v[8:9], v[8:9], 0, s[36:37]
	s_lshl_b32 s57, s25, 6
	s_lshl_b32 s25, s25, 13
	s_lshl_b32 s26, s34, 12
	s_waitcnt vmcnt(4)
	s_barrier
	global_load_lds_dwordx4 v[8:9], off
	v_lshl_add_u64 v[6:7], v[6:7], 0, s[36:37]
	s_add_i32 m0, s51, 0x1a000
	s_add_i32 s58, s51, 0x8000
	s_add_i32 s59, s51, 0xa000
	global_load_lds_dwordx4 v[6:7], off
	v_lshl_add_u64 v[4:5], v[4:5], 0, s[36:37]
	s_mov_b32 m0, s58
	s_add_u32 s0, s40, 0x30080
	global_load_lds_dwordx4 v[4:5], off
	v_lshl_add_u64 v[2:3], v[2:3], 0, s[36:37]
	s_mov_b32 m0, s59
	s_addc_u32 s1, s41, 0
	global_load_lds_dwordx4 v[2:3], off
	s_add_i32 m0, s51, 0x1c000
	v_lshl_add_u64 v[2:3], s[0:1], 0, v[178:179]
	global_load_lds_dwordx4 v[2:3], off
	v_lshl_add_u64 v[2:3], s[0:1], 0, v[182:183]
	s_add_i32 m0, s51, 0x1e000
	s_lshl_b32 s61, s33, 3
	global_load_lds_dwordx4 v[2:3], off
	s_abs_i32 s62, s61
	v_and_b32_e32 v227, 15, v0
	v_and_b32_e32 v2, 48, v0
	v_lshlrev_b32_e32 v4, 2, v0
	v_lshlrev_b32_e32 v5, 6, v0
	v_bfe_u32 v229, v0, 3, 3
	v_cvt_f32_u32_e32 v0, s62
	s_abs_i32 s64, s33
	v_cvt_f32_u32_e32 v6, s64
	s_movk_i32 s0, 0x3c0
	v_rcp_iflag_f32_e32 v0, v0
	s_mulk_i32 s24, 0x900
	v_rcp_iflag_f32_e32 v6, v6
	v_and_or_b32 v5, v5, s0, v2
	v_mul_f32_e32 v0, 0x4f7ffffe, v0
	v_cvt_u32_f32_e32 v0, v0
	s_add_i32 s0, s24, 0
	v_lshl_or_b32 v3, v227, 6, v2
	v_and_b32_e32 v4, 32, v4
	s_add_i32 s0, s0, 0x20000
	v_bitop3_b32 v3, v3, s25, v4 bitop3:0xde
	v_bitop3_b32 v228, s26, v5, v4 bitop3:0xf6
	s_movk_i32 s1, 0x90
	v_mov_b32_e32 v4, s0
	v_mad_u32_u24 v5, v227, s1, v4
	v_mad_u32_u24 v4, v229, s1, v4
	v_readfirstlane_b32 s1, v0
	v_mul_f32_e32 v0, 0x4f7ffffe, v6
	v_cvt_u32_f32_e32 v0, v0
	s_sub_i32 s0, 0, s62
	s_mul_i32 s0, s0, s1
	s_mul_hi_u32 s0, s1, s0
	s_add_i32 s66, s1, s0
	s_sub_i32 s0, 0, s64
	v_readfirstlane_b32 s1, v0
	v_add_u16_e32 v0, v1, v10
	s_waitcnt vmcnt(6)
	s_mul_i32 s0, s0, s1
	v_lshrrev_b16_e32 v0, 1, v0
	v_and_b32_e32 v230, 0x70, v13
	s_mul_hi_u32 s0, s1, s0
	v_add_lshl_u32 v184, v11, v0, 1
	v_add_lshl_u32 v186, v12, v0, 1
	s_add_i32 s69, 0, 0x10000
	s_add_i32 s70, 0, 0x14000
	v_mbcnt_lo_u32_b32 v0, -1, 0
	s_mov_b32 s27, 0x20000
	s_lshl_b32 s60, s34, 6
	s_waitcnt lgkmcnt(0)
	s_ashr_i32 s63, s55, 31
	s_mov_b32 s26, 0x6000000
	s_and_b32 s25, s9, 0xffff
	s_mov_b32 s24, s8
	s_bfe_i32 s65, s33, 0x1001c
	s_ashr_i32 s67, s33, 31
	s_add_i32 s68, s1, s0
	v_mov_b32_e32 v185, v179
	v_mov_b32_e32 v187, v179
	v_mov_b64_e32 v[188:189], s[6:7]
	v_add_u32_e32 v231, s69, v228
	v_add_u32_e32 v232, 0, v3
	v_add_u32_e32 v233, s70, v228
	s_movk_i32 s71, 0x600
	s_movk_i32 s72, 0x300
	v_mbcnt_hi_u32_b32 v234, -1, v0
	v_add_u32_e32 v235, v5, v2
	v_add_u32_e32 v236, v4, v230
	s_movk_i32 s73, 0x60
	s_mov_b32 s74, 0x30000
	s_mov_b32 s75, 0x36000
	s_lshl_b32 s34, s34, 3
	s_movk_i32 s76, 0x3000
	s_mov_b32 s77, 0x3c000
	s_mov_b32 s78, 0x42000
	s_movk_i32 s79, 0x1000
	s_mov_b32 s80, s35
	s_barrier
	s_cmpk_gt_u32 s44, 0xff
	s_cbranch_scc0 .Lprio10_done
.Lprio10_done:
.LBB10_12:
	s_add_i32 s80, s80, 1
	s_mul_i32 s0, s80, s63
	s_mul_hi_u32 s1, s80, s55
	s_add_i32 s1, s1, s0
	s_mul_i32 s0, s80, s55
	s_add_u32 s0, s0, s2
	s_addc_u32 s1, s1, s47
	v_cmp_ge_i64_e32 vcc, s[0:1], v[188:189]
	s_and_b64 s[6:7], exec, vcc
	s_mov_b64 vcc, s[6:7]
	s_cbranch_vccnz .LBB10_22
	s_ashr_i32 s8, s0, 31
	s_lshr_b32 s8, s8, 29
	s_add_i32 s42, s0, s8
	s_and_b32 s8, s42, -8
	s_sub_i32 s43, s0, s8
	s_cmp_ge_i32 s43, s46
	s_mov_b64 s[8:9], -1
	s_cbranch_scc0 .LBB10_15
	s_sub_i32 s8, s43, s46
	s_mul_i32 s8, s8, s45
	s_add_i32 s81, s8, s49
	s_mov_b64 s[8:9], 0
